# baseline (speedup 1.0000x reference)
_Z8moe_gemmILi1024ELi2048ELb1EEvPKDF16_S1_PKfPDF16_PfPKiS7_:
	v_lshl_or_b32 v216, s2, 8, v0
	v_and_b32_e32 v217, 63, v216
	v_lshrrev_b32_e32 v216, 6, v216
	v_lshlrev_b32_e32 v215, 3, v217
	v_lshlrev_b32_e32 v214, 4, v217
	v_lshl_add_u32 v217, v216, 10, v215
	v_lshl_add_u32 v216, v216, 11, v214
	s_mov_b32 s96, 16
	s_mov_b32 s97, 0
	s_mov_b32 s98, 0
	s_and_b32 s90, s2, 7
	s_lshr_b32 s91, s2, 3
	v_readfirstlane_b32 s88, v0
	s_load_dwordx2 s[4:5], s[0:1], 0x28
	v_readfirstlane_b32 s12, v0
	s_waitcnt lgkmcnt(0)
	s_load_dwordx2 s[92:93], s[4:5], 0x400
	s_add_u32 s94, s4, 0x6000000
	s_addc_u32 s95, s5, 0
	s_load_dword s23, s[4:5], 0x0
	s_load_dword s25, s[4:5], 0x80
	s_load_dword s27, s[4:5], 0x100
	s_load_dword s29, s[4:5], 0x180
	s_load_dword s31, s[4:5], 0x200
	s_load_dword s33, s[4:5], 0x280
	s_load_dword s35, s[4:5], 0x300
	s_load_dword s38, s[4:5], 0x380
	s_waitcnt lgkmcnt(0)
	global_load_dwordx4 v[218:221], v216, s[92:93] nt
	global_load_dwordx4 v[222:225], v216, s[92:93] offset:1024 nt
	s_add_u32 s92, s92, 0x400000
	s_addc_u32 s93, s93, 0
	global_load_dwordx4 v[226:229], v216, s[92:93] nt
	global_load_dwordx4 v[230:233], v216, s[92:93] offset:1024 nt
	s_add_u32 s92, s92, 0x400000
	s_addc_u32 s93, s93, 0
	global_load_dwordx4 v[234:237], v216, s[92:93] nt
	global_load_dwordx4 v[238:241], v216, s[92:93] offset:1024 nt
	s_add_u32 s92, s92, 0x400000
	s_addc_u32 s93, s93, 0
	global_load_dwordx4 v[242:245], v216, s[92:93] nt
	global_load_dwordx4 v[246:249], v216, s[92:93] offset:1024 nt
	s_add_u32 s92, s92, 0x400000
	s_addc_u32 s93, s93, 0
	s_mov_b32 s100, 1
	s_add_i32 s3, s23, 0x9f
	s_mul_hi_i32 s3, s3, 0x66666667
	s_lshr_b32 s4, s3, 31
	s_ashr_i32 s39, s3, 6
	s_add_i32 s3, s25, 0x9f
	s_mul_hi_i32 s3, s3, 0x66666667
	s_add_i32 s39, s39, s4
	s_lshr_b32 s4, s3, 31
	s_ashr_i32 s40, s3, 6
	s_add_i32 s40, s40, s4
	s_add_i32 s4, s27, 0x9f
	s_mul_hi_i32 s4, s4, 0x66666667
	s_lshr_b32 s5, s4, 31
	s_ashr_i32 s41, s4, 6
	s_add_i32 s4, s29, 0x9f
	s_mul_hi_i32 s4, s4, 0x66666667
	s_add_i32 s41, s41, s5
	s_lshr_b32 s5, s4, 31
	s_ashr_i32 s42, s4, 6
	s_add_i32 s4, s31, 0x9f
	s_mul_hi_i32 s4, s4, 0x66666667
	s_add_i32 s42, s42, s5
	s_lshr_b32 s5, s4, 31
	s_ashr_i32 s43, s4, 6
	s_add_i32 s4, s33, 0x9f
	s_mul_hi_i32 s4, s4, 0x66666667
	s_add_i32 s3, s40, s39
	s_add_i32 s43, s43, s5
	s_lshr_b32 s5, s4, 31
	s_ashr_i32 s44, s4, 6
	s_add_i32 s4, s35, 0x9f
	s_add_i32 s3, s41, s3
	s_mul_hi_i32 s4, s4, 0x66666667
	s_add_i32 s3, s42, s3
	s_add_i32 s44, s44, s5
	s_lshr_b32 s5, s4, 31
	s_ashr_i32 s45, s4, 6
	s_add_i32 s4, s38, 0x9f
	s_add_i32 s3, s43, s3
	s_mul_hi_i32 s4, s4, 0x66666667
	s_add_i32 s3, s44, s3
	s_add_i32 s45, s45, s5
	s_lshr_b32 s5, s4, 31
	s_ashr_i32 s46, s4, 6
	s_add_i32 s3, s45, s3
	s_add_i32 s46, s46, s5
	s_add_i32 s3, s46, s3
	s_lshl_b32 s3, s3, 4
	s_and_b32 s4, s2, 7
	s_mul_i32 s4, s3, s4
	s_lshr_b32 s2, s2, 3
	s_ashr_i32 s5, s4, 3
	s_add_i32 s4, s4, s3
	s_ashr_i32 s47, s4, 3
	s_add_i32 s48, s5, s2
	s_sub_i32 s89, s47, s5
	s_sub_i32 s89, s89, 64
	s_max_i32 s89, s89, 0
	s_min_i32 s89, s89, 64
	s_add_i32 s99, s48, 64
	s_cmp_lt_i32 s99, s47
	s_cselect_b32 s98, 1, 0
	s_cmp_eq_u32 s98, 0
	s_cbranch_scc1 .Las_set
	s_cmp_ge_i32 s89, 64
	s_cbranch_scc1 .Las_set
	s_mov_b32 s96, 8
	s_mov_b32 s98, 1073741824

.Lw2k_p0:
	s_cmp_lt_u32 s96, 4
	s_cbranch_scc1 .Lpf_nob
	s_cmp_lg_u32 s98, 0x40000000
	s_cbranch_scc1 .Lpf_nob
	s_cmp_lg_u32 s100, 0
	s_cbranch_scc1 .Lpf_nob
	global_load_dwordx4 v[218:221], v216, s[92:93] nt
	global_load_dwordx4 v[222:225], v216, s[92:93] offset:1024 nt
	s_add_u32 s92, s92, 0x400000
	s_addc_u32 s93, s93, 0
	global_load_dwordx4 v[226:229], v216, s[92:93] nt
	global_load_dwordx4 v[230:233], v216, s[92:93] offset:1024 nt
	s_add_u32 s92, s92, 0x400000
	s_addc_u32 s93, s93, 0
	global_load_dwordx4 v[234:237], v216, s[92:93] nt
	global_load_dwordx4 v[238:241], v216, s[92:93] offset:1024 nt
	s_add_u32 s92, s92, 0x400000
	s_addc_u32 s93, s93, 0
	global_load_dwordx4 v[242:245], v216, s[92:93] nt
	global_load_dwordx4 v[246:249], v216, s[92:93] offset:1024 nt
	s_add_u32 s92, s92, 0x400000
	s_addc_u32 s93, s93, 0
	s_sub_u32 s96, s96, 4
	s_mov_b32 s100, 1
